# v101 + k3 head-norm statistics: the 32 ds_bpermute cross-row shuffles replaced by v_permlane16/32_swap pairs (no LDS round trips); k6 LN1 exchange: L1 invalidate after the partner poll dropped (partne
# baseline (speedup 1.0000x reference)
.LBB0_810:
	v_and_b32_e32 v133, 64, v249
	v_xor_b32_e32 v132, 16, v249
	v_add_u32_e32 v136, 64, v133
	v_cmp_lt_i32_e32 vcc, v132, v136
	v_mul_f32_e32 v134, v129, v129
	v_fmac_f32_e32 v134, v128, v128
	v_cndmask_b32_e32 v132, v249, v132, vcc
	v_lshlrev_b32_e32 v137, 2, v132
	v_add_f32_e32 v132, 0, v128
	v_add_f32_e32 v132, v129, v132
	v_add_f32_e32 v132, v130, v132
	v_add_f32_e32 v132, v131, v132
	v_add_f32_e32 v135, v124, v132
	v_mov_b32_e32 v132, v124
	v_mov_b32_e32 v133, v131
	v_fmac_f32_e32 v134, v130, v130
	v_pk_mul_f32 v[132:133], v[132:133], v[132:133]
	s_mov_b64 s[58:59], s[44:45]
	v_add_f32_e32 v133, v133, v134
	v_add_f32_e32 v138, v132, v133
	v_add_f32_e32 v132, v125, v135
	v_add_f32_e32 v139, v126, v132
	v_pk_mul_f32 v[132:133], v[126:127], v[126:127]
	v_pk_mul_f32 v[134:135], v[124:125], v[124:125]
	s_nop 0
	v_add_f32_e32 v133, v135, v138
	v_add_f32_e32 v134, v132, v133
	v_add_f32_e32 v132, v127, v139
	v_add_f32_e32 v135, v132, v120
	v_pk_mov_b32 v[132:133], v[126:127], v[120:121] op_sel:[1,0]
	s_nop 0
	v_pk_mul_f32 v[132:133], v[132:133], v[132:133]
	s_nop 0
	v_add_f32_e32 v132, v132, v134
	v_add_f32_e32 v138, v132, v133
	v_add_f32_e32 v132, v121, v135
	v_add_f32_e32 v139, v122, v132
	v_pk_mul_f32 v[132:133], v[122:123], v[122:123]
	v_pk_mul_f32 v[134:135], v[120:121], v[120:121]
	s_nop 0
	v_add_f32_e32 v133, v135, v138
	v_add_f32_e32 v134, v132, v133
	v_add_f32_e32 v132, v123, v139
	v_add_f32_e32 v135, v116, v132
	v_mov_b32_e32 v132, v116
	v_mov_b32_e32 v133, v123
	v_pk_mul_f32 v[132:133], v[132:133], v[132:133]
	v_pk_mul_f32 v[138:139], v[116:117], v[116:117]
	v_add_f32_e32 v133, v133, v134
	v_add_f32_e32 v133, v132, v133
	v_add_f32_e32 v132, v117, v135
	v_pk_mul_f32 v[134:135], v[118:119], v[118:119]
	v_add_f32_e32 v133, v139, v133
	v_add_f32_e32 v132, v118, v132
	v_add_f32_e32 v135, v134, v133
	v_mul_f32_e32 v133, v119, v119
	v_mov_b32_e32 v134, v119
	v_pk_add_f32 v[132:133], v[134:135], v[132:133]
	v_mov_b32_e32 v134, v132
	v_mov_b32_e32 v135, v133
	s_nop 1
	v_permlane16_swap_b32_e32 v134, v132
	v_permlane16_swap_b32_e32 v135, v133
	v_xor_b32_e32 v138, 32, v249
	v_cmp_lt_i32_e32 vcc, v138, v136
	s_waitcnt lgkmcnt(0)
	v_pk_add_f32 v[132:133], v[132:133], v[134:135]
	v_cndmask_b32_e32 v136, v249, v138, vcc
	v_lshlrev_b32_e32 v139, 2, v136
	v_mov_b32_e32 v134, v132
	v_mov_b32_e32 v135, v133
	s_nop 1
	v_permlane32_swap_b32_e32 v134, v132
	v_permlane32_swap_b32_e32 v135, v133
	v_mov_b32_e32 v136, v205
	s_nop 0
	v_lshl_add_u32 v138, v136, 5, s94
	s_and_saveexec_b64 s[26:27], s[38:39]
	s_cbranch_execz .LBB0_812
	s_waitcnt lgkmcnt(0)
	v_pk_add_f32 v[132:133], v[132:133], v[134:135]
	ds_write_b64 v138, v[132:133]
.LBB0_812:
	s_or_b64 exec, exec, s[26:27]
	v_add_f32_e32 v132, 0, v112
	v_add_f32_e32 v132, v113, v132
	v_add_f32_e32 v132, v114, v132
	s_waitcnt lgkmcnt(0)
	v_mul_f32_e32 v134, v113, v113
	v_add_f32_e32 v132, v115, v132
	v_fmac_f32_e32 v134, v112, v112
	v_add_f32_e32 v135, v108, v132
	v_mov_b32_e32 v132, v108
	v_mov_b32_e32 v133, v115
	v_fmac_f32_e32 v134, v114, v114
	v_pk_mul_f32 v[132:133], v[132:133], v[132:133]
	s_nop 0
	v_add_f32_e32 v133, v133, v134
	v_add_f32_e32 v140, v132, v133
	v_add_f32_e32 v132, v109, v135
	v_add_f32_e32 v141, v110, v132
	v_pk_mul_f32 v[132:133], v[110:111], v[110:111]
	v_pk_mul_f32 v[134:135], v[108:109], v[108:109]
	s_nop 0
	v_add_f32_e32 v133, v135, v140
	v_add_f32_e32 v134, v132, v133
	v_add_f32_e32 v132, v111, v141
	v_add_f32_e32 v135, v132, v104
	v_pk_mov_b32 v[132:133], v[110:111], v[104:105] op_sel:[1,0]
	s_nop 0
	v_pk_mul_f32 v[132:133], v[132:133], v[132:133]
	s_nop 0
	v_add_f32_e32 v132, v132, v134
	v_add_f32_e32 v140, v132, v133
	v_add_f32_e32 v132, v105, v135
	v_add_f32_e32 v141, v106, v132
	v_pk_mul_f32 v[132:133], v[106:107], v[106:107]
	v_pk_mul_f32 v[134:135], v[104:105], v[104:105]
	s_nop 0
	v_add_f32_e32 v133, v135, v140
	v_add_f32_e32 v134, v132, v133
	v_add_f32_e32 v132, v107, v141
	v_add_f32_e32 v135, v100, v132
	v_mov_b32_e32 v132, v100
	v_mov_b32_e32 v133, v107
	v_pk_mul_f32 v[132:133], v[132:133], v[132:133]
	v_pk_mul_f32 v[140:141], v[100:101], v[100:101]
	v_add_f32_e32 v133, v133, v134
	v_add_f32_e32 v133, v132, v133
	v_add_f32_e32 v132, v101, v135
	v_pk_mul_f32 v[134:135], v[102:103], v[102:103]
	v_add_f32_e32 v133, v141, v133
	v_add_f32_e32 v132, v102, v132
	v_add_f32_e32 v135, v134, v133
	v_mul_f32_e32 v133, v103, v103
	v_mov_b32_e32 v134, v103
	v_pk_add_f32 v[132:133], v[134:135], v[132:133]
	v_mov_b32_e32 v134, v132
	v_mov_b32_e32 v135, v133
	s_nop 1
	v_permlane16_swap_b32_e32 v134, v132
	v_permlane16_swap_b32_e32 v135, v133
	s_waitcnt lgkmcnt(0)
	v_pk_add_f32 v[132:133], v[132:133], v[134:135]
	v_mov_b32_e32 v134, v132
	v_mov_b32_e32 v135, v133
	s_nop 1
	v_permlane32_swap_b32_e32 v134, v132
	v_permlane32_swap_b32_e32 v135, v133
	s_and_saveexec_b64 s[26:27], s[38:39]
	s_cbranch_execz .LBB0_814
	s_waitcnt lgkmcnt(0)
	v_pk_add_f32 v[132:133], v[132:133], v[134:135]
	ds_write_b64 v138, v[132:133] offset:512
.LBB0_814:
	s_or_b64 exec, exec, s[26:27]
	v_add_f32_e32 v132, 0, v96
	v_add_f32_e32 v132, v97, v132
	v_add_f32_e32 v132, v98, v132
	s_waitcnt lgkmcnt(0)
	v_mul_f32_e32 v134, v97, v97
	v_add_f32_e32 v132, v99, v132
	v_fmac_f32_e32 v134, v96, v96
	v_add_f32_e32 v135, v92, v132
	v_mov_b32_e32 v132, v92
	v_mov_b32_e32 v133, v99
	v_fmac_f32_e32 v134, v98, v98
	v_pk_mul_f32 v[132:133], v[132:133], v[132:133]
	s_nop 0
	v_add_f32_e32 v133, v133, v134
	v_add_f32_e32 v140, v132, v133
	v_add_f32_e32 v132, v93, v135
	v_add_f32_e32 v141, v94, v132
	v_pk_mul_f32 v[132:133], v[94:95], v[94:95]
	v_pk_mul_f32 v[134:135], v[92:93], v[92:93]
	s_nop 0
	v_add_f32_e32 v133, v135, v140
	v_add_f32_e32 v134, v132, v133
	v_add_f32_e32 v132, v95, v141
	v_add_f32_e32 v135, v132, v88
	v_pk_mov_b32 v[132:133], v[94:95], v[88:89] op_sel:[1,0]
	s_nop 0
	v_pk_mul_f32 v[132:133], v[132:133], v[132:133]
	s_nop 0
	v_add_f32_e32 v132, v132, v134
	v_add_f32_e32 v140, v132, v133
	v_add_f32_e32 v132, v89, v135
	v_add_f32_e32 v141, v90, v132
	v_pk_mul_f32 v[132:133], v[90:91], v[90:91]
	v_pk_mul_f32 v[134:135], v[88:89], v[88:89]
	s_nop 0
	v_add_f32_e32 v133, v135, v140
	v_add_f32_e32 v134, v132, v133
	v_add_f32_e32 v132, v91, v141
	v_add_f32_e32 v135, v84, v132
	v_mov_b32_e32 v132, v84
	v_mov_b32_e32 v133, v91
	v_pk_mul_f32 v[132:133], v[132:133], v[132:133]
	v_pk_mul_f32 v[140:141], v[84:85], v[84:85]
	v_add_f32_e32 v133, v133, v134
	v_add_f32_e32 v133, v132, v133
	v_add_f32_e32 v132, v85, v135
	v_pk_mul_f32 v[134:135], v[86:87], v[86:87]
	v_add_f32_e32 v133, v141, v133
	v_add_f32_e32 v132, v86, v132
	v_add_f32_e32 v135, v134, v133
	v_mul_f32_e32 v133, v87, v87
	v_mov_b32_e32 v134, v87
	v_pk_add_f32 v[132:133], v[134:135], v[132:133]
	v_mov_b32_e32 v134, v132
	v_mov_b32_e32 v135, v133
	s_nop 1
	v_permlane16_swap_b32_e32 v134, v132
	v_permlane16_swap_b32_e32 v135, v133
	s_waitcnt lgkmcnt(0)
	v_pk_add_f32 v[132:133], v[132:133], v[134:135]
	v_mov_b32_e32 v134, v132
	v_mov_b32_e32 v135, v133
	s_nop 1
	v_permlane32_swap_b32_e32 v134, v132
	v_permlane32_swap_b32_e32 v135, v133
	s_and_saveexec_b64 s[26:27], s[38:39]
	s_cbranch_execz .LBB0_816
	s_waitcnt lgkmcnt(0)
	v_pk_add_f32 v[132:133], v[132:133], v[134:135]
	ds_write_b64 v138, v[132:133] offset:1024
.LBB0_816:
	s_or_b64 exec, exec, s[26:27]
	v_add_f32_e32 v132, 0, v80
	v_add_f32_e32 v132, v81, v132
	v_add_f32_e32 v132, v82, v132
	s_waitcnt lgkmcnt(0)
	v_mul_f32_e32 v134, v81, v81
	v_add_f32_e32 v132, v83, v132
	v_fmac_f32_e32 v134, v80, v80
	v_add_f32_e32 v135, v76, v132
	v_mov_b32_e32 v132, v76
	v_mov_b32_e32 v133, v83
	v_fmac_f32_e32 v134, v82, v82
	v_pk_mul_f32 v[132:133], v[132:133], v[132:133]
	s_nop 0
	v_add_f32_e32 v133, v133, v134
	v_add_f32_e32 v140, v132, v133
	v_add_f32_e32 v132, v77, v135
	v_add_f32_e32 v141, v78, v132
	v_pk_mul_f32 v[132:133], v[78:79], v[78:79]
	v_pk_mul_f32 v[134:135], v[76:77], v[76:77]
	s_nop 0
	v_add_f32_e32 v133, v135, v140
	v_add_f32_e32 v134, v132, v133
	v_add_f32_e32 v132, v79, v141
	v_add_f32_e32 v135, v132, v72
	v_pk_mov_b32 v[132:133], v[78:79], v[72:73] op_sel:[1,0]
	s_nop 0
	v_pk_mul_f32 v[132:133], v[132:133], v[132:133]
	s_nop 0
	v_add_f32_e32 v132, v132, v134
	v_add_f32_e32 v140, v132, v133
	v_add_f32_e32 v132, v73, v135
	v_add_f32_e32 v141, v74, v132
	v_pk_mul_f32 v[132:133], v[74:75], v[74:75]
	v_pk_mul_f32 v[134:135], v[72:73], v[72:73]
	s_nop 0
	v_add_f32_e32 v133, v135, v140
	v_add_f32_e32 v134, v132, v133
	v_add_f32_e32 v132, v75, v141
	v_add_f32_e32 v135, v68, v132
	v_mov_b32_e32 v132, v68
	v_mov_b32_e32 v133, v75
	v_pk_mul_f32 v[132:133], v[132:133], v[132:133]
	v_pk_mul_f32 v[140:141], v[68:69], v[68:69]
	v_add_f32_e32 v133, v133, v134
	v_add_f32_e32 v133, v132, v133
	v_add_f32_e32 v132, v69, v135
	v_pk_mul_f32 v[134:135], v[70:71], v[70:71]
	v_add_f32_e32 v133, v141, v133
	v_add_f32_e32 v132, v70, v132
	v_add_f32_e32 v135, v134, v133
	v_mul_f32_e32 v133, v71, v71
	v_mov_b32_e32 v134, v71
	v_pk_add_f32 v[132:133], v[134:135], v[132:133]
	v_mov_b32_e32 v134, v132
	v_mov_b32_e32 v135, v133
	s_nop 1
	v_permlane16_swap_b32_e32 v134, v132
	v_permlane16_swap_b32_e32 v135, v133
	s_waitcnt lgkmcnt(0)
	v_pk_add_f32 v[132:133], v[132:133], v[134:135]
	v_mov_b32_e32 v134, v132
	v_mov_b32_e32 v135, v133
	s_nop 1
	v_permlane32_swap_b32_e32 v134, v132
	v_permlane32_swap_b32_e32 v135, v133
	s_and_saveexec_b64 s[26:27], s[38:39]
	s_cbranch_execz .LBB0_818
	s_waitcnt lgkmcnt(0)
	v_pk_add_f32 v[132:133], v[132:133], v[134:135]
	ds_write_b64 v138, v[132:133] offset:1536
.LBB0_818:
	s_or_b64 exec, exec, s[26:27]
	v_add_f32_e32 v132, 0, v62
	v_add_f32_e32 v132, v63, v132
	v_add_f32_e32 v132, v64, v132
	s_waitcnt lgkmcnt(0)
	v_mul_f32_e32 v134, v63, v63
	v_add_f32_e32 v132, v65, v132
	v_fmac_f32_e32 v134, v62, v62
	v_add_f32_e32 v135, v58, v132
	v_mov_b32_e32 v132, v58
	v_mov_b32_e32 v133, v65
	v_fmac_f32_e32 v134, v64, v64
	v_pk_mul_f32 v[132:133], v[132:133], v[132:133]
	s_nop 0
	v_add_f32_e32 v133, v133, v134
	v_add_f32_e32 v140, v132, v133
	v_add_f32_e32 v132, v59, v135
	v_add_f32_e32 v141, v60, v132
	v_pk_mul_f32 v[132:133], v[60:61], v[60:61]
	v_pk_mul_f32 v[134:135], v[58:59], v[58:59]
	s_nop 0
	v_add_f32_e32 v133, v135, v140
	v_add_f32_e32 v134, v132, v133
	v_add_f32_e32 v132, v61, v141
	v_add_f32_e32 v135, v132, v54
	v_pk_mov_b32 v[132:133], v[60:61], v[54:55] op_sel:[1,0]
	s_nop 0
	v_pk_mul_f32 v[132:133], v[132:133], v[132:133]
	s_nop 0
	v_add_f32_e32 v132, v132, v134
	v_add_f32_e32 v140, v132, v133
	v_add_f32_e32 v132, v55, v135
	v_add_f32_e32 v141, v56, v132
	v_pk_mul_f32 v[132:133], v[56:57], v[56:57]
	v_pk_mul_f32 v[134:135], v[54:55], v[54:55]
	s_nop 0
	v_add_f32_e32 v133, v135, v140
	v_add_f32_e32 v134, v132, v133
	v_add_f32_e32 v132, v57, v141
	v_add_f32_e32 v135, v50, v132
	v_mov_b32_e32 v132, v50
	v_mov_b32_e32 v133, v57
	v_pk_mul_f32 v[132:133], v[132:133], v[132:133]
	v_pk_mul_f32 v[140:141], v[50:51], v[50:51]
	v_add_f32_e32 v133, v133, v134
	v_add_f32_e32 v133, v132, v133
	v_add_f32_e32 v132, v51, v135
	v_pk_mul_f32 v[134:135], v[52:53], v[52:53]
	v_add_f32_e32 v133, v141, v133
	v_add_f32_e32 v132, v52, v132
	v_add_f32_e32 v135, v134, v133
	v_mul_f32_e32 v133, v53, v53
	v_mov_b32_e32 v134, v53
	v_pk_add_f32 v[132:133], v[134:135], v[132:133]
	v_mov_b32_e32 v134, v132
	v_mov_b32_e32 v135, v133
	s_nop 1
	v_permlane16_swap_b32_e32 v134, v132
	v_permlane16_swap_b32_e32 v135, v133
	s_waitcnt lgkmcnt(0)
	v_pk_add_f32 v[132:133], v[132:133], v[134:135]
	v_mov_b32_e32 v134, v132
	v_mov_b32_e32 v135, v133
	s_nop 1
	v_permlane32_swap_b32_e32 v134, v132
	v_permlane32_swap_b32_e32 v135, v133
	s_and_saveexec_b64 s[26:27], s[38:39]
	s_cbranch_execz .LBB0_820
	s_waitcnt lgkmcnt(0)
	v_pk_add_f32 v[132:133], v[132:133], v[134:135]
	ds_write_b64 v138, v[132:133] offset:4096
.LBB0_820:
	s_or_b64 exec, exec, s[26:27]
	v_add_f32_e32 v132, 0, v46
	v_add_f32_e32 v132, v47, v132
	v_add_f32_e32 v132, v48, v132
	s_waitcnt lgkmcnt(0)
	v_mul_f32_e32 v134, v47, v47
	v_add_f32_e32 v132, v49, v132
	v_fmac_f32_e32 v134, v46, v46
	v_add_f32_e32 v135, v42, v132
	v_mov_b32_e32 v132, v42
	v_mov_b32_e32 v133, v49
	v_fmac_f32_e32 v134, v48, v48
	v_pk_mul_f32 v[132:133], v[132:133], v[132:133]
	s_nop 0
	v_add_f32_e32 v133, v133, v134
	v_add_f32_e32 v140, v132, v133
	v_add_f32_e32 v132, v43, v135
	v_add_f32_e32 v141, v44, v132
	v_pk_mul_f32 v[132:133], v[44:45], v[44:45]
	v_pk_mul_f32 v[134:135], v[42:43], v[42:43]
	s_nop 0
	v_add_f32_e32 v133, v135, v140
	v_add_f32_e32 v134, v132, v133
	v_add_f32_e32 v132, v45, v141
	v_add_f32_e32 v135, v132, v38
	v_pk_mov_b32 v[132:133], v[44:45], v[38:39] op_sel:[1,0]
	s_nop 0
	v_pk_mul_f32 v[132:133], v[132:133], v[132:133]
	s_nop 0
	v_add_f32_e32 v132, v132, v134
	v_add_f32_e32 v140, v132, v133
	v_add_f32_e32 v132, v39, v135
	v_add_f32_e32 v141, v40, v132
	v_pk_mul_f32 v[132:133], v[40:41], v[40:41]
	v_pk_mul_f32 v[134:135], v[38:39], v[38:39]
	s_nop 0
	v_add_f32_e32 v133, v135, v140
	v_add_f32_e32 v134, v132, v133
	v_add_f32_e32 v132, v41, v141
	v_add_f32_e32 v135, v34, v132
	v_mov_b32_e32 v132, v34
	v_mov_b32_e32 v133, v41
	v_pk_mul_f32 v[132:133], v[132:133], v[132:133]
	v_pk_mul_f32 v[140:141], v[34:35], v[34:35]
	v_add_f32_e32 v133, v133, v134
	v_add_f32_e32 v133, v132, v133
	v_add_f32_e32 v132, v35, v135
	v_pk_mul_f32 v[134:135], v[36:37], v[36:37]
	v_add_f32_e32 v133, v141, v133
	v_add_f32_e32 v132, v36, v132
	v_add_f32_e32 v135, v134, v133
	v_mul_f32_e32 v133, v37, v37
	v_mov_b32_e32 v134, v37
	v_pk_add_f32 v[132:133], v[134:135], v[132:133]
	v_mov_b32_e32 v134, v132
	v_mov_b32_e32 v135, v133
	s_nop 1
	v_permlane16_swap_b32_e32 v134, v132
	v_permlane16_swap_b32_e32 v135, v133
	s_waitcnt lgkmcnt(0)
	v_pk_add_f32 v[132:133], v[132:133], v[134:135]
	v_mov_b32_e32 v134, v132
	v_mov_b32_e32 v135, v133
	s_nop 1
	v_permlane32_swap_b32_e32 v134, v132
	v_permlane32_swap_b32_e32 v135, v133
	s_and_saveexec_b64 s[26:27], s[38:39]
	s_cbranch_execz .LBB0_822
	s_waitcnt lgkmcnt(0)
	v_pk_add_f32 v[132:133], v[132:133], v[134:135]
	ds_write_b64 v138, v[132:133] offset:4608
.LBB0_822:
	s_or_b64 exec, exec, s[26:27]
	v_add_f32_e32 v132, 0, v30
	v_add_f32_e32 v132, v31, v132
	v_add_f32_e32 v132, v32, v132
	s_waitcnt lgkmcnt(0)
	v_mul_f32_e32 v134, v31, v31
	v_add_f32_e32 v132, v33, v132
	v_fmac_f32_e32 v134, v30, v30
	v_add_f32_e32 v135, v26, v132
	v_mov_b32_e32 v132, v26
	v_mov_b32_e32 v133, v33
	v_fmac_f32_e32 v134, v32, v32
	v_pk_mul_f32 v[132:133], v[132:133], v[132:133]
	s_nop 0
	v_add_f32_e32 v133, v133, v134
	v_add_f32_e32 v140, v132, v133
	v_add_f32_e32 v132, v27, v135
	v_add_f32_e32 v141, v28, v132
	v_pk_mul_f32 v[132:133], v[28:29], v[28:29]
	v_pk_mul_f32 v[134:135], v[26:27], v[26:27]
	s_nop 0
	v_add_f32_e32 v133, v135, v140
	v_add_f32_e32 v134, v132, v133
	v_add_f32_e32 v132, v29, v141
	v_add_f32_e32 v135, v132, v22
	v_pk_mov_b32 v[132:133], v[28:29], v[22:23] op_sel:[1,0]
	s_nop 0
	v_pk_mul_f32 v[132:133], v[132:133], v[132:133]
	s_nop 0
	v_add_f32_e32 v132, v132, v134
	v_add_f32_e32 v140, v132, v133
	v_add_f32_e32 v132, v23, v135
	v_add_f32_e32 v141, v24, v132
	v_pk_mul_f32 v[132:133], v[24:25], v[24:25]
	v_pk_mul_f32 v[134:135], v[22:23], v[22:23]
	s_nop 0
	v_add_f32_e32 v133, v135, v140
	v_add_f32_e32 v134, v132, v133
	v_add_f32_e32 v132, v25, v141
	v_add_f32_e32 v135, v18, v132
	v_mov_b32_e32 v132, v18
	v_mov_b32_e32 v133, v25
	v_pk_mul_f32 v[132:133], v[132:133], v[132:133]
	v_pk_mul_f32 v[140:141], v[18:19], v[18:19]
	v_add_f32_e32 v133, v133, v134
	v_add_f32_e32 v133, v132, v133
	v_add_f32_e32 v132, v19, v135
	v_pk_mul_f32 v[134:135], v[20:21], v[20:21]
	v_add_f32_e32 v133, v141, v133
	v_add_f32_e32 v132, v20, v132
	v_add_f32_e32 v135, v134, v133
	v_mul_f32_e32 v133, v21, v21
	v_mov_b32_e32 v134, v21
	v_pk_add_f32 v[132:133], v[134:135], v[132:133]
	v_mov_b32_e32 v134, v132
	v_mov_b32_e32 v135, v133
	s_nop 1
	v_permlane16_swap_b32_e32 v134, v132
	v_permlane16_swap_b32_e32 v135, v133
	s_waitcnt lgkmcnt(0)
	v_pk_add_f32 v[132:133], v[132:133], v[134:135]
	v_mov_b32_e32 v134, v132
	v_mov_b32_e32 v135, v133
	s_nop 1
	v_permlane32_swap_b32_e32 v134, v132
	v_permlane32_swap_b32_e32 v135, v133
	s_and_saveexec_b64 s[26:27], s[38:39]
	s_cbranch_execz .LBB0_824
	s_waitcnt lgkmcnt(0)
	v_pk_add_f32 v[132:133], v[132:133], v[134:135]
	ds_write_b64 v138, v[132:133] offset:5120
.LBB0_824:
	s_or_b64 exec, exec, s[26:27]
	v_add_f32_e32 v132, 0, v14
	v_add_f32_e32 v132, v15, v132
	v_add_f32_e32 v132, v16, v132
	s_waitcnt lgkmcnt(0)
	v_mul_f32_e32 v134, v15, v15
	v_add_f32_e32 v132, v17, v132
	v_fmac_f32_e32 v134, v14, v14
	v_add_f32_e32 v135, v10, v132
	v_mov_b32_e32 v132, v10
	v_mov_b32_e32 v133, v17
	v_fmac_f32_e32 v134, v16, v16
	v_pk_mul_f32 v[132:133], v[132:133], v[132:133]
	s_nop 0
	v_add_f32_e32 v133, v133, v134
	v_add_f32_e32 v140, v132, v133
	v_add_f32_e32 v132, v11, v135
	v_add_f32_e32 v141, v12, v132
	v_pk_mul_f32 v[132:133], v[12:13], v[12:13]
	v_pk_mul_f32 v[134:135], v[10:11], v[10:11]
	s_nop 0
	v_add_f32_e32 v133, v135, v140
	v_add_f32_e32 v134, v132, v133
	v_add_f32_e32 v132, v13, v141
	v_add_f32_e32 v135, v132, v6
	v_pk_mov_b32 v[132:133], v[12:13], v[6:7] op_sel:[1,0]
	s_nop 0
	v_pk_mul_f32 v[132:133], v[132:133], v[132:133]
	s_nop 0
	v_add_f32_e32 v132, v132, v134
	v_add_f32_e32 v140, v132, v133
	v_add_f32_e32 v132, v7, v135
	v_add_f32_e32 v141, v8, v132
	v_pk_mul_f32 v[132:133], v[8:9], v[8:9]
	v_pk_mul_f32 v[134:135], v[6:7], v[6:7]
	s_nop 0
	v_add_f32_e32 v133, v135, v140
	v_add_f32_e32 v134, v132, v133
	v_add_f32_e32 v132, v9, v141
	v_add_f32_e32 v135, v2, v132
	v_mov_b32_e32 v132, v2
	v_mov_b32_e32 v133, v9
	v_pk_mul_f32 v[132:133], v[132:133], v[132:133]
	v_pk_mul_f32 v[140:141], v[2:3], v[2:3]
	v_add_f32_e32 v133, v133, v134
	v_add_f32_e32 v133, v132, v133
	v_add_f32_e32 v132, v3, v135
	v_pk_mul_f32 v[134:135], v[4:5], v[4:5]
	v_add_f32_e32 v133, v141, v133
	v_add_f32_e32 v132, v4, v132
	v_add_f32_e32 v135, v134, v133
	v_mul_f32_e32 v133, v5, v5
	v_mov_b32_e32 v134, v5
	v_pk_add_f32 v[132:133], v[134:135], v[132:133]
	v_mov_b32_e32 v134, v132
	v_mov_b32_e32 v135, v133
	s_nop 1
	v_permlane16_swap_b32_e32 v134, v132
	v_permlane16_swap_b32_e32 v135, v133
	s_waitcnt lgkmcnt(0)
	v_pk_add_f32 v[132:133], v[132:133], v[134:135]
	v_mov_b32_e32 v134, v132
	v_mov_b32_e32 v135, v133
	s_nop 1
	v_permlane32_swap_b32_e32 v134, v132
	v_permlane32_swap_b32_e32 v135, v133
	s_and_saveexec_b64 s[26:27], s[38:39]
	s_cbranch_execz .LBB0_826
	s_waitcnt lgkmcnt(0)
	v_pk_add_f32 v[132:133], v[132:133], v[134:135]
	ds_write_b64 v138, v[132:133] offset:5632
